# v65 + P11 conversion item second form: 8 x dwordx4 loads + 8 x ds_write_b128 into a 36-dword-pitch transpose image, lane constants kept in v250-v255 across queries (~190 instr per item)
# speedup vs baseline: 1.0144x; 1.0027x over previous
.LBB0_1449:
	s_or_b64 exec, exec, s[16:17]
	v_ashrrev_i32_e32 v1, 31, v0
	v_lshl_add_u64 v[2:3], v[0:1], 2, s[14:15]
	global_load_dword v2, v[2:3], off
	v_lshl_add_u32 v1, v0, 2, 0
	v_add_u32_e32 v1, 0x24000, v1
	v_cmp_gt_i32_e32 vcc, 16, v0
	s_waitcnt vmcnt(0)
	v_mul_f32_e32 v2, 0x3fb8aa3b, v2
	ds_write_b32 v1, v2
	s_and_saveexec_b64 s[2:3], vcc
	v_mov_b32_e32 v0, 0xff800000
	ds_write_b32 v1, v0 offset:2048
	s_or_b64 exec, exec, s[2:3]
	s_lshl_b32 s2, s93, 14
	s_add_i32 s23, s2, 0
	s_lshl_b32 s2, s88, 3
	s_add_i32 s15, s2, s93
	s_lshl_b32 s22, s96, 3
	s_cmpk_gt_i32 s15, 0x7fff
	s_waitcnt lgkmcnt(0)
	s_barrier
	s_cbranch_scc1 .LBB0_1478
	s_add_u32 s24, s0, 0x12c00000
	s_addc_u32 s25, s1, 0
	s_add_u32 s26, s0, 0x28000000
	s_addc_u32 s27, s1, 0
	s_add_u32 s4, s0, 0x27000000
	s_addc_u32 s5, s1, 0
	s_add_u32 s28, s0, 0x26000000
	s_addc_u32 s29, s1, 0
	s_lshl_b32 s2, s93, 9
	v_and_b32_e32 v159, 64, v6
	s_add_i32 s30, s2, 0
	s_lshl_b32 s2, s93, 8
	v_xor_b32_e32 v0, 16, v6
	v_add_u32_e32 v1, 64, v159
	s_add_i32 s37, s2, 0
	v_cmp_lt_i32_e32 vcc, v0, v1
	s_add_i32 s30, s30, 0x20000
	s_add_i32 s31, s37, 0x21000
	v_cndmask_b32_e32 v0, v6, v0, vcc
	v_lshlrev_b32_e32 v160, 2, v0
	v_xor_b32_e32 v0, 32, v6
	s_add_u32 s33, s0, 0xa000000
	v_cmp_lt_i32_e32 vcc, v0, v1
	s_addc_u32 s34, s1, 0
	s_add_u32 s35, s0, 0x2000000
	v_cndmask_b32_e32 v0, v6, v0, vcc
	s_mov_b32 s7, 0
	v_lshlrev_b32_e32 v161, 2, v0
	s_addc_u32 s36, s1, 0
	s_add_i32 s37, s37, 0x21010
	v_mov_b32_e32 v1, 0
	s_add_i32 s38, 0, 0x24000
	s_mov_b32 s14, 0x3a800000
	s_mov_b32 s39, 0xc3e00000
	s_movk_i32 s40, 0x84
	v_mov_b32_e32 v162, 0x43e00000
	s_lshl_b32 s41, s22, 1
	s_lshl_b32 s42, s22, 5
	s_mov_b32 s43, 0
	v_and_b32_e32 v163, 15, v158
	v_ashrrev_i32_e32 v164, 4, v158
	v_lshl_add_u32 v189, v163, 2, s38
	v_lshlrev_b32_e32 v6, 2, v164
	v_lshlrev_b32_e32 v0, 1, v158
	v_bfe_u32 v5, v158, 2, 2
	v_and_b32_e32 v0, 14, v0
	v_bfe_u32 v4, v158, 3, 1
	v_or_b32_e32 v5, v6, v5
	v_lshlrev_b32_e32 v2, 1, v164
	v_lshlrev_b32_e32 v7, 1, v5
	v_lshlrev_b32_e32 v9, 3, v158
	v_bitop3_b32 v10, v0, v2, v4 bitop3:0x36
	v_or_b32_e32 v11, 1, v2
	v_add_u32_e32 v12, 8, v2
	v_add_u32_e32 v13, 9, v2
	v_add_u32_e32 v14, 16, v2
	v_add_u32_e32 v15, 17, v2
	v_add_u32_e32 v16, 24, v2
	v_add_u32_e32 v2, 25, v2
	v_and_b32_e32 v7, 14, v7
	v_bfe_u32 v8, v164, 1, 1
	v_and_or_b32 v9, v9, 8, s23
	v_bfe_u32 v3, v158, 1, 1
	v_bitop3_b32 v11, v0, v11, v4 bitop3:0x36
	v_bitop3_b32 v12, v0, v12, v4 bitop3:0x36
	v_bitop3_b32 v13, v13, v0, v4 bitop3:0x1e
	v_bitop3_b32 v14, v0, v14, v4 bitop3:0x36
	v_bitop3_b32 v15, v15, v0, v4 bitop3:0x1e
	v_bitop3_b32 v16, v0, v16, v4 bitop3:0x36
	v_bitop3_b32 v0, v2, v0, v4 bitop3:0x1e
	v_lshl_add_u32 v5, v5, 9, v9
	v_lshlrev_b32_e32 v4, 4, v0
	v_bitop3_b32 v0, v7, v3, v8 bitop3:0x36
	v_lshl_add_u32 v177, v0, 4, v5
	v_or_b32_e32 v0, 2, v3
	v_bitop3_b32 v0, v7, v0, v8 bitop3:0x36
	v_lshl_add_u32 v178, v0, 4, v5
	v_or_b32_e32 v0, 4, v3
	v_bitop3_b32 v0, v7, v0, v8 bitop3:0x36
	v_lshl_add_u32 v179, v0, 4, v5
	v_or_b32_e32 v0, 6, v3
	v_bitop3_b32 v0, v7, v0, v8 bitop3:0x36
	v_lshl_add_u32 v180, v0, 4, v5
	v_or_b32_e32 v0, 8, v3
	v_bitop3_b32 v0, v7, v0, v8 bitop3:0x36
	v_lshl_add_u32 v181, v0, 4, v5
	v_or_b32_e32 v0, 10, v3
	v_bitop3_b32 v0, v7, v0, v8 bitop3:0x36
	v_lshl_add_u32 v182, v0, 4, v5
	v_or_b32_e32 v0, 12, v3
	v_bitop3_b32 v0, v7, v0, v8 bitop3:0x36
	v_lshl_add_u32 v183, v0, 4, v5
	v_or_b32_e32 v0, 14, v3
	v_bitop3_b32 v0, v7, v0, v8 bitop3:0x36
	v_lshl_add_u32 v184, v0, 4, v5
	v_or_b32_e32 v0, 16, v3
	v_bitop3_b32 v0, v7, v0, v8 bitop3:0x36
	v_lshl_add_u32 v175, v0, 4, v5
	v_or_b32_e32 v0, 18, v3
	v_bitop3_b32 v0, v7, v0, v8 bitop3:0x36
	v_lshl_add_u32 v176, v0, 4, v5
	v_or_b32_e32 v0, 20, v3
	v_bitop3_b32 v0, v7, v0, v8 bitop3:0x36
	v_lshl_add_u32 v174, v0, 4, v5
	v_or_b32_e32 v0, 22, v3
	v_bitop3_b32 v0, v7, v0, v8 bitop3:0x36
	v_lshl_add_u32 v172, v0, 4, v5
	v_or_b32_e32 v0, 24, v3
	v_bitop3_b32 v0, v7, v0, v8 bitop3:0x36
	v_lshl_add_u32 v173, v0, 4, v5
	v_or_b32_e32 v0, 26, v3
	v_bitop3_b32 v0, v7, v0, v8 bitop3:0x36
	v_lshl_add_u32 v171, v0, 4, v5
	v_or_b32_e32 v0, 28, v3
	v_bitop3_b32 v0, v7, v0, v8 bitop3:0x36
	v_lshl_add_u32 v169, v0, 4, v5
	v_or_b32_e32 v0, 30, v3
	v_bitop3_b32 v0, v7, v0, v8 bitop3:0x36
	v_lshl_add_u32 v9, v163, 9, s23
	v_lshlrev_b32_e32 v10, 4, v10
	v_lshlrev_b32_e32 v11, 4, v11
	v_lshlrev_b32_e32 v12, 4, v12
	v_lshlrev_b32_e32 v13, 4, v13
	v_lshlrev_b32_e32 v14, 4, v14
	v_lshlrev_b32_e32 v15, 4, v15
	v_lshlrev_b32_e32 v16, 4, v16
	v_lshl_add_u32 v170, v0, 4, v5
	v_and_or_b32 v0, v6, 60, v159
	v_lshlrev_b32_e32 v167, 2, v0
	v_add_u32_e32 v193, v9, v10
	v_add_u32_e32 v194, v9, v11
	v_add_u32_e32 v190, v9, v12
	v_add_u32_e32 v191, v9, v13
	v_add_u32_e32 v192, v9, v14
	v_add_u32_e32 v186, v9, v15
	v_add_u32_e32 v187, v9, v16
	v_add_u32_e32 v188, v9, v4
	v_or_b32_e32 v168, 4, v167
	v_or_b32_e32 v165, 8, v167
	v_or_b32_e32 v166, 12, v167
	v_lshrrev_b32_e32 v250, 3, v158
	v_and_b32_e32 v251, 7, v158
	v_lshlrev_b32_e32 v251, 4, v251
	v_mul_u32_u24_e32 v252, 0x90, v250
	v_add3_u32 v252, v252, v251, s23
	v_and_b32_e32 v253, 31, v158
	v_lshlrev_b32_e32 v255, 10, v253
	v_lshlrev_b32_e32 v253, 2, v253
	v_and_b32_e32 v0, 32, v158
	v_add_u32_e32 v255, v255, v0
	v_mul_u32_u24_e32 v0, 0x90, v0
	v_add3_u32 v253, v253, v0, s23
	s_mov_b32 s16, s15
	s_branch .LBB0_1454

.Lcv11_cm:
	s_lshl_b32 s46, s20, 2
	s_add_u32 s2, s2, s46
	s_addc_u32 s3, s3, 0
	v_add_u32_e32 v2, s6, v250
	v_lshlrev_b32_e32 v2, s21, v2
	v_add_u32_e32 v2, v2, v251
	s_lshl_b32 s46, 8, s21
	s_lshl_b32 s20, s20, 10
	v_mov_b32_e32 v41, s6
	v_add3_u32 v40, v255, s20, v41
	global_load_dwordx4 v[8:11], v2, s[2:3]
	v_add_u32_e32 v3, s46, v2
	global_load_dwordx4 v[12:15], v3, s[2:3]
	v_add_u32_e32 v2, s46, v3
	global_load_dwordx4 v[16:19], v2, s[2:3]
	v_add_u32_e32 v3, s46, v2
	global_load_dwordx4 v[20:23], v3, s[2:3]
	v_add_u32_e32 v2, s46, v3
	global_load_dwordx4 v[24:27], v2, s[2:3]
	v_add_u32_e32 v3, s46, v2
	global_load_dwordx4 v[28:31], v3, s[2:3]
	v_add_u32_e32 v2, s46, v3
	global_load_dwordx4 v[32:35], v2, s[2:3]
	v_add_u32_e32 v3, s46, v2
	global_load_dwordx4 v[36:39], v3, s[2:3]
	s_waitcnt vmcnt(7)
	v_mul_f32_e32 v8, 0x42800000, v8
	v_mul_f32_e32 v9, 0x42800000, v9
	v_mul_f32_e32 v10, 0x42800000, v10
	v_mul_f32_e32 v11, 0x42800000, v11
	ds_write_b128 v252, v[8:11]
	s_waitcnt vmcnt(6)
	v_mul_f32_e32 v12, 0x42800000, v12
	v_mul_f32_e32 v13, 0x42800000, v13
	v_mul_f32_e32 v14, 0x42800000, v14
	v_mul_f32_e32 v15, 0x42800000, v15
	ds_write_b128 v252, v[12:15] offset:1152
	s_waitcnt vmcnt(5)
	v_mul_f32_e32 v16, 0x42800000, v16
	v_mul_f32_e32 v17, 0x42800000, v17
	v_mul_f32_e32 v18, 0x42800000, v18
	v_mul_f32_e32 v19, 0x42800000, v19
	ds_write_b128 v252, v[16:19] offset:2304
	s_waitcnt vmcnt(4)
	v_mul_f32_e32 v20, 0x42800000, v20
	v_mul_f32_e32 v21, 0x42800000, v21
	v_mul_f32_e32 v22, 0x42800000, v22
	v_mul_f32_e32 v23, 0x42800000, v23
	ds_write_b128 v252, v[20:23] offset:3456
	s_waitcnt vmcnt(3)
	v_mul_f32_e32 v24, 0x42800000, v24
	v_mul_f32_e32 v25, 0x42800000, v25
	v_mul_f32_e32 v26, 0x42800000, v26
	v_mul_f32_e32 v27, 0x42800000, v27
	ds_write_b128 v252, v[24:27] offset:4608
	s_waitcnt vmcnt(2)
	v_mul_f32_e32 v28, 0x42800000, v28
	v_mul_f32_e32 v29, 0x42800000, v29
	v_mul_f32_e32 v30, 0x42800000, v30
	v_mul_f32_e32 v31, 0x42800000, v31
	ds_write_b128 v252, v[28:31] offset:5760
	s_waitcnt vmcnt(1)
	v_mul_f32_e32 v32, 0x42800000, v32
	v_mul_f32_e32 v33, 0x42800000, v33
	v_mul_f32_e32 v34, 0x42800000, v34
	v_mul_f32_e32 v35, 0x42800000, v35
	ds_write_b128 v252, v[32:35] offset:6912
	s_waitcnt vmcnt(0)
	v_mul_f32_e32 v36, 0x42800000, v36
	v_mul_f32_e32 v37, 0x42800000, v37
	v_mul_f32_e32 v38, 0x42800000, v38
	v_mul_f32_e32 v39, 0x42800000, v39
	ds_write_b128 v252, v[36:39] offset:8064
	s_waitcnt lgkmcnt(0)
	ds_read2_b32 v[8:9], v253 offset0:0 offset1:36
	ds_read2_b32 v[10:11], v253 offset0:72 offset1:108
	ds_read2_b32 v[12:13], v253 offset0:144 offset1:180
	ds_read2_b32 v[14:15], v253 offset0:216 offset1:252
	v_add_u32_e32 v41, 0x480, v253
	ds_read2_b32 v[16:17], v41 offset0:0 offset1:36
	ds_read2_b32 v[18:19], v41 offset0:72 offset1:108
	ds_read2_b32 v[20:21], v41 offset0:144 offset1:180
	ds_read2_b32 v[22:23], v41 offset0:216 offset1:252
	v_add_u32_e32 v41, 0x900, v253
	ds_read2_b32 v[24:25], v41 offset0:0 offset1:36
	ds_read2_b32 v[26:27], v41 offset0:72 offset1:108
	ds_read2_b32 v[28:29], v41 offset0:144 offset1:180
	ds_read2_b32 v[30:31], v41 offset0:216 offset1:252
	v_add_u32_e32 v41, 0xd80, v253
	ds_read2_b32 v[32:33], v41 offset0:0 offset1:36
	ds_read2_b32 v[34:35], v41 offset0:72 offset1:108
	ds_read2_b32 v[36:37], v41 offset0:144 offset1:180
	ds_read2_b32 v[38:39], v41 offset0:216 offset1:252
	s_waitcnt lgkmcnt(14)
	v_med3_f32 v8, v8, s39, v162
	v_med3_f32 v9, v9, s39, v162
	v_med3_f32 v10, v10, s39, v162
	v_med3_f32 v11, v11, s39, v162
	v_cvt_pk_fp8_f32 v42, v8, v9
	v_cvt_pk_fp8_f32 v42, v10, v11 op_sel:[0,0,1]
	s_waitcnt lgkmcnt(12)
	v_med3_f32 v12, v12, s39, v162
	v_med3_f32 v13, v13, s39, v162
	v_med3_f32 v14, v14, s39, v162
	v_med3_f32 v15, v15, s39, v162
	v_cvt_pk_fp8_f32 v43, v12, v13
	v_cvt_pk_fp8_f32 v43, v14, v15 op_sel:[0,0,1]
	s_waitcnt lgkmcnt(10)
	v_med3_f32 v16, v16, s39, v162
	v_med3_f32 v17, v17, s39, v162
	v_med3_f32 v18, v18, s39, v162
	v_med3_f32 v19, v19, s39, v162
	v_cvt_pk_fp8_f32 v44, v16, v17
	v_cvt_pk_fp8_f32 v44, v18, v19 op_sel:[0,0,1]
	s_waitcnt lgkmcnt(8)
	v_med3_f32 v20, v20, s39, v162
	v_med3_f32 v21, v21, s39, v162
	v_med3_f32 v22, v22, s39, v162
	v_med3_f32 v23, v23, s39, v162
	v_cvt_pk_fp8_f32 v45, v20, v21
	v_cvt_pk_fp8_f32 v45, v22, v23 op_sel:[0,0,1]
	global_store_dwordx4 v40, v[42:45], s[18:19]
	s_nop 1
	s_waitcnt lgkmcnt(6)
	v_med3_f32 v24, v24, s39, v162
	v_med3_f32 v25, v25, s39, v162
	v_med3_f32 v26, v26, s39, v162
	v_med3_f32 v27, v27, s39, v162
	v_cvt_pk_fp8_f32 v42, v24, v25
	v_cvt_pk_fp8_f32 v42, v26, v27 op_sel:[0,0,1]
	s_waitcnt lgkmcnt(4)
	v_med3_f32 v28, v28, s39, v162
	v_med3_f32 v29, v29, s39, v162
	v_med3_f32 v30, v30, s39, v162
	v_med3_f32 v31, v31, s39, v162
	v_cvt_pk_fp8_f32 v43, v28, v29
	v_cvt_pk_fp8_f32 v43, v30, v31 op_sel:[0,0,1]
	s_waitcnt lgkmcnt(2)
	v_med3_f32 v32, v32, s39, v162
	v_med3_f32 v33, v33, s39, v162
	v_med3_f32 v34, v34, s39, v162
	v_med3_f32 v35, v35, s39, v162
	v_cvt_pk_fp8_f32 v44, v32, v33
	v_cvt_pk_fp8_f32 v44, v34, v35 op_sel:[0,0,1]
	s_waitcnt lgkmcnt(0)
	v_med3_f32 v36, v36, s39, v162
	v_med3_f32 v37, v37, s39, v162
	v_med3_f32 v38, v38, s39, v162
	v_med3_f32 v39, v39, s39, v162
	v_cvt_pk_fp8_f32 v45, v36, v37
	v_cvt_pk_fp8_f32 v45, v38, v39 op_sel:[0,0,1]
	global_store_dwordx4 v40, v[42:45], s[18:19] offset:16
	s_branch .LBB0_1472
